# P10 K-loop: LDS-DMA issue balanced 4/4/4/4 over the four load segments (was 2/6/2/6), on top of v65
# speedup vs baseline: 1.0029x; 1.0029x over previous
;     DI unsigned rowoff(const Unit& u, int r) const { return (unsigned)(u.pm * BM + r) * (unsigned)K2; }
;     DI unsigned rowoff(const Unit& u, int r) const { if (GATHER) return sroff[u.pm * BM + r]; else return (unsigned)(u.pm * BM + r) * (unsigned)K2; }
; #define PG8_STAGE(bufoff, gbase, voff) do { _Pragma("unroll") for (int _i = 0; _i < 2; ++_i) \
;         __builtin_amdgcn_global_load_lds((const unsigned*)((const char*)(gbase) + (voff)[_i]), (LAS unsigned*)(lds + (bufoff) + ldsw + _i * 8192), 16, 0, 0); } while (0)
; #define PG8_WAIT_V(n) asm volatile("s_waitcnt vmcnt(" #n ")" ::: "memory")
; #define PG8_BAR __builtin_amdgcn_s_barrier()
;     const int tid = threadIdx.x, wid = __builtin_amdgcn_readfirstlane(tid >> 6), lane = tid & 63, wr = wid >> 2, wc = wid & 3, fr = lane & 15, fq = lane >> 4;
;     const int K = g.K, nt = K / BK;
;     int stR[2]; unsigned stC2[2], voffB[2];
; #pragma unroll
;     for (int i = 0; i < 2; ++i) { int R, C; stage_rc(tid * 16 + i * 8192, R, C); const int Rb = Epi::PERM ? ((R & ~31) + perm32(R & 31)) : R;
;         stR[i] = R; stC2[i] = (unsigned)C * 2u; voffB[i] = (unsigned)(Rb * K + C) * 2u; }
;     const size_t kstep = (size_t)(BK * 2);
;     const size_t hstep = (size_t)HALF * K * 2;
;     const unsigned ldsw = (unsigned)wid * 1024u;
;     const int aoffL = lds_byte(wr * 64 + fr, fq * 8), boffL = lds_byte(wc * 32 + fr, fq * 8);
;     ...
;     for (int i = 0; i < 2; ++i) { ao0[i] = S.rowoff(cur, stR[i]) + stC2[i]; ao1[i] = S.rowoff(cur, HALF + stR[i]) + stC2[i]; no0[i] = ao0[i]; no1[i] = ao1[i]; }
;     const char* Ab = (const char*)g.A;
;     const char* cB = (const char*)g.Bt + (size_t)cur.brow * K * 2;
;     if constexpr (SP2) {
;         PG8_STAGE(PG8_SB(0, 0), cB, voffB); PG8_STAGE(PG8_SB(0, 1), cB + hstep, voffB); PG8_STAGE(PG8_SA(0, 0), Ab, ao0); PG8_STAGE(PG8_SA(0, 1), Ab, ao1);
;         if (wr == 1) PG8_BAR;
;         PG8_WAIT_V(2); PG8_BAR;
;         PG8_STAGE(PG8_SB(1, 0), cB + kstep, voffB); PG8_STAGE(PG8_SA(1, 0), Ab + kstep, ao0); PG8_STAGE(PG8_SB(1, 1), cB + hstep + kstep, voffB);
;         PG8_WAIT_V(6); PG8_BAR;
.LBB0_2262:
	s_lshl_b32 s18, s18, 5
	s_and_b32 s37, s18, 0x60
	s_lshl_b32 s36, s25, 13
	s_lshl_b32 s51, s37, 7
	s_add_u32 s18, s12, 0x3ae00000
	s_mov_b64 s[20:21], 0x80
	s_addc_u32 s19, s13, 0
	s_add_i32 m0, s61, 0x18000
	v_lshl_add_u64 v[4:5], v[4:5], 0, s[20:21]
	s_waitcnt vmcnt(2)
	s_barrier
	global_load_lds_dwordx4 v[4:5], off
	s_add_i32 m0, s61, 0x1a000
	s_add_u32 s22, s12, 0x36c00080
	v_lshl_add_u64 v[2:3], v[2:3], 0, s[20:21]
	s_addc_u32 s23, s13, 0
	s_add_i32 s66, s61, 0x8000
	s_add_i32 s67, s61, 0xa000
	global_load_lds_dwordx4 v[2:3], off
	v_lshl_add_u64 v[2:3], s[22:23], 0, v[158:159]
	s_mov_b32 m0, s66
	s_add_u32 s34, s8, 0x40080
	global_load_lds_dwordx4 v[2:3], off
	v_lshl_add_u64 v[2:3], s[22:23], 0, v[78:79]
	s_mov_b32 m0, s67
	s_addc_u32 s35, s9, 0
	global_load_lds_dwordx4 v[2:3], off
	v_lshl_add_u64 v[250:251], s[22:23], 0, v[158:159]
	v_lshl_add_u64 v[252:253], s[22:23], 0, v[78:79]
	s_add_i32 m0, s61, 0x1c000
	v_lshl_add_u64 v[2:3], s[34:35], 0, v[154:155]
	global_load_lds_dwordx4 v[2:3], off
	v_lshl_add_u64 v[2:3], s[34:35], 0, v[156:157]
	s_add_i32 m0, s61, 0x1e000
	v_mov_b32_e32 v5, v159
	global_load_lds_dwordx4 v[2:3], off
	v_and_b32_e32 v2, 15, v0
	v_lshl_or_b32 v163, s25, 6, v2
	v_lshlrev_b32_e32 v3, 1, v8
	v_lshlrev_b32_e32 v180, 2, v163
	v_lshl_or_b32 v2, v2, 6, v3
	v_and_b32_e32 v4, 32, v180
	v_bitop3_b32 v9, v2, s36, v4 bitop3:0xde
	v_lshlrev_b32_e32 v2, 6, v0
	s_movk_i32 s25, 0x3c0
	v_and_or_b32 v2, v2, s25, v3
	v_lshlrev_b32_e32 v3, 2, v0
	v_and_b32_e32 v3, 32, v3
	v_lshlrev_b32_e32 v4, 4, v162
	v_bitop3_b32 v181, s51, v2, v3 bitop3:0xf6
	s_waitcnt vmcnt(6)
	v_lshl_add_u64 v[160:161], s[30:31], 0, v[4:5]
	v_lshl_add_u64 v[166:167], s[26:27], 0, v[4:5]
	v_mov_b32_e32 v3, s7
	v_mov_b32_e32 v4, s5
	v_cmp_gt_u32_e32 vcc, 32, v162
	s_cmpk_lt_u32 s24, 0x100
	v_or_b32_e32 v182, s37, v8
	v_and_b32_e32 v2, 0x7c, v164
	v_cndmask_b32_e32 v169, v3, v4, vcc
	v_mov_b32_e32 v3, s6
	v_mov_b32_e32 v4, s4
	s_mov_b32 s68, 0
	s_mov_b32 s69, 0x18000
	s_mov_b32 s70, 0x8000
	v_mov_b32_e32 v165, v159
	s_cselect_b64 s[24:25], -1, 0
	v_lshlrev_b32_e32 v183, 2, v182
	v_lshlrev_b32_e32 v184, 2, v6
	v_lshlrev_b32_e32 v185, 2, v7
	s_ashr_i32 s71, s33, 3
	v_cndmask_b32_e32 v168, v3, v4, vcc
	v_cndmask_b32_e64 v186, 0, 1, s[28:29]
	s_add_i32 s72, 0, 0x10000
	s_add_i32 s73, 0, 0x14000
	v_add_u32_e32 v187, 0, v9
	s_mov_b32 s74, 0xc0c00000
	s_mov_b32 s75, 0x40000
	s_mov_b32 s76, 0x48000
	s_mov_b32 s77, 0x50000
	v_lshlrev_b32_e32 v170, 2, v2
	v_mov_b32_e32 v188, 0x41000000
	v_mov_b32_e32 v79, v158
	s_mov_b32 s78, s2
	s_barrier
	s_branch .LBB0_2265

; #define LAS __attribute__((address_space(3)))
; #define PG8_STAGE(bufoff, gbase, voff) do { _Pragma("unroll") for (int _i = 0; _i < 2; ++_i) \
;         __builtin_amdgcn_global_load_lds((const unsigned*)((const char*)(gbase) + (voff)[_i]), (LAS unsigned*)(lds + (bufoff) + ldsw + _i * 8192), 16, 0, 0); } while (0)
; #define PG8_LDA(dst, b, h) do { _Pragma("unroll") for (int m = 0; m < 4; ++m) _Pragma("unroll") for (int k = 0; k < 2; ++k) dst[m][k] = *(const LAS bf16x8*)(lds + PG8_SA(b, h) + aoffL + m * 2048 + k * 1024); } while (0)
; #define PG8_LDB(dst, b, h) do { _Pragma("unroll") for (int n = 0; n < 2; ++n) _Pragma("unroll") for (int k = 0; k < 2; ++k) dst[n][k] = *(const LAS bf16x8*)(lds + PG8_SB(b, h) + boffL + n * 2048 + k * 1024); } while (0)
; #define PG8_WAIT_V(n) asm volatile("s_waitcnt vmcnt(" #n ")" ::: "memory")
; #define PG8_WAIT_L(n) asm volatile("s_waitcnt lgkmcnt(" #n ")" ::: "memory")
;     ...
;         for (int t = 0; t < nt; t += 2) {
;             const bool last = (t == nt - 2);
;             if constexpr (Epi::HOOK) { if (t == nt / 2) E.hook(acc, cur, wr, wc, fr, fq); }
;             const char* a1 = Ab + (size_t)(t + 1) * kstep;
;             const char* a2 = last ? Ab : Ab + (size_t)(t + 2) * kstep; const char* b2 = last ? nB : cB + (size_t)(t + 2) * kstep;
;             const char* a3 = a2 + kstep; const char* b3 = b2 + kstep;
;             if constexpr (Sched::GATHER) { if (last && has_next) { const LAS unsigned char* gs = xgo + ((ui + 1) & 1) * 1024;
; #pragma unroll
;                 for (int i = 0; i < 2; ++i) { no0[i] = *(const LAS unsigned*)(gs + 4 * stR[i]) + stC2[i]; no1[i] = *(const LAS unsigned*)(gs + 4 * (HALF + stR[i])) + stC2[i]; } } }
;             unsigned x0[2], x1[2];
; #pragma unroll
;             for (int i = 0; i < 2; ++i) { x0[i] = last ? no0[i] : ao0[i]; x1[i] = last ? no1[i] : ao1[i]; }
;             if constexpr (SP2) {
;             PG8_LDB(B0, 0, 0); PG8_LDB(B1, 0, 1); PG8_SCHED; PG8_LDA(At, 0, 0); PG8_STAGE(PG8_SA(1, 1), a1, ao1);
;             PG8_WAIT_V(8); PG8_WAIT_L(0); PG8_BAR; PG8_MMA(0, 0, At, B0); PG8_MMA(0, 1, At, B1); PG8_BAR; PG8_SCHED;
;             PG8_LDA(At, 0, 1); PG8_STAGE(PG8_SB(0, 0), b2, voffB); PG8_STAGE(PG8_SB(0, 1), b2 + hstep, voffB); PG8_STAGE(PG8_SA(0, 0), a2, x0);
;             PG8_WAIT_V(8); PG8_WAIT_L(0); PG8_BAR; PG8_MMA(1, 0, At, B0); PG8_MMA(1, 1, At, B1); PG8_BAR; PG8_SCHED;
.LBB0_2282:
	v_add_u32_e32 v88, s72, v181
	s_add_u32 s34, s12, s30
	ds_read_b128 v[98:101], v88
	ds_read_b128 v[102:105], v88 offset:1024
	ds_read_b128 v[106:109], v88 offset:2048
	ds_read_b128 v[172:175], v88 offset:3072
	v_add_u32_e32 v88, s73, v181
	s_addc_u32 s35, s13, s31
	ds_read_b128 v[176:179], v88
	ds_read_b128 v[194:197], v88 offset:1024
	ds_read_b128 v[198:201], v88 offset:2048
	ds_read_b128 v[202:205], v88 offset:3072
	s_add_u32 s36, s34, 0x36c00100
	s_addc_u32 s37, s35, 0
	s_and_b64 s[34:35], s[8:9], exec
	s_cselect_b32 s37, s15, s37
	s_cselect_b32 s36, s14, s36
	s_add_u32 s54, s51, s30
	s_addc_u32 s55, s52, s31
	s_and_b64 s[34:35], s[8:9], exec
	s_cselect_b32 s35, s27, s55
	s_cselect_b32 s34, s26, s54
	v_cndmask_b32_e64 v158, v79, v189, s[8:9]
	v_cndmask_b32_e64 v171, v80, v190, s[8:9]
	v_cndmask_b32_e64 v238, v78, v191, s[8:9]
	v_cndmask_b32_e64 v193, v82, v192, s[8:9]
	v_lshl_add_u64 v[88:89], v[86:87], 0, s[30:31]
	s_mov_b32 m0, s66
	ds_read_b128 v[206:209], v187
	ds_read_b128 v[210:213], v187 offset:1024
	ds_read_b128 v[214:217], v187 offset:2048
	ds_read_b128 v[218:221], v187 offset:3072
	ds_read_b128 v[222:225], v187 offset:4096
	ds_read_b128 v[226:229], v187 offset:5120
	ds_read_b128 v[230:233], v187 offset:6144
	ds_read_b128 v[234:237], v187 offset:7168
	global_load_lds_dwordx4 v[250:251], off
	s_mov_b32 m0, s67
	s_nop 0
	global_load_lds_dwordx4 v[252:253], off
	s_add_i32 m0, s61, 0xc000
	s_nop 0
	global_load_lds_dwordx4 v[88:89], off
	v_lshl_add_u64 v[88:89], v[84:85], 0, s[30:31]
	s_add_i32 m0, s61, 0xe000
	s_nop 0
	global_load_lds_dwordx4 v[88:89], off
	s_waitcnt vmcnt(8)
	s_waitcnt lgkmcnt(0)
	s_barrier
	s_setprio 1
	s_waitcnt lgkmcnt(0)
	v_mfma_i32_16x16x64_i8 v[150:153], v[98:101], v[206:209], v[150:153]
	v_mfma_i32_16x16x64_i8 v[142:145], v[106:109], v[206:209], v[142:145]
	v_mfma_i32_16x16x64_i8 v[134:137], v[98:101], v[214:217], v[134:137]
	v_mfma_i32_16x16x64_i8 v[126:129], v[106:109], v[214:217], v[126:129]
	v_mfma_i32_16x16x64_i8 v[118:121], v[98:101], v[222:225], v[118:121]
	v_mfma_i32_16x16x64_i8 v[110:113], v[106:109], v[222:225], v[110:113]
	v_mfma_i32_16x16x64_i8 v[88:91], v[98:101], v[230:233], v[90:93]
	v_mfma_i32_16x16x64_i8 v[70:73], v[106:109], v[230:233], v[70:73]
	v_mfma_i32_16x16x64_i8 v[150:153], v[102:105], v[210:213], v[150:153]
	v_mfma_i32_16x16x64_i8 v[142:145], v[172:175], v[210:213], v[142:145]
	v_mfma_i32_16x16x64_i8 v[134:137], v[102:105], v[218:221], v[134:137]
	v_mfma_i32_16x16x64_i8 v[126:129], v[172:175], v[218:221], v[126:129]
	v_mfma_i32_16x16x64_i8 v[118:121], v[102:105], v[226:229], v[118:121]
	v_mfma_i32_16x16x64_i8 v[110:113], v[172:175], v[226:229], v[110:113]
	v_mfma_i32_16x16x64_i8 v[88:91], v[102:105], v[234:237], v[88:91]
	v_mfma_i32_16x16x64_i8 v[70:73], v[172:175], v[234:237], v[70:73]
	s_setprio 0
	s_setprio 1
	v_mfma_i32_16x16x64_i8 v[146:149], v[176:179], v[206:209], v[146:149]
	v_mfma_i32_16x16x64_i8 v[138:141], v[198:201], v[206:209], v[138:141]
	v_mfma_i32_16x16x64_i8 v[130:133], v[176:179], v[214:217], v[130:133]
	v_mfma_i32_16x16x64_i8 v[122:125], v[198:201], v[214:217], v[122:125]
	v_mfma_i32_16x16x64_i8 v[114:117], v[176:179], v[222:225], v[114:117]
	v_mfma_i32_16x16x64_i8 v[92:95], v[198:201], v[222:225], v[94:97]
	v_mfma_i32_16x16x64_i8 v[74:77], v[176:179], v[230:233], v[74:77]
	v_mfma_i32_16x16x64_i8 v[66:69], v[198:201], v[230:233], v[66:69]
	v_mfma_i32_16x16x64_i8 v[146:149], v[194:197], v[210:213], v[146:149]
	v_mfma_i32_16x16x64_i8 v[138:141], v[202:205], v[210:213], v[138:141]
	v_mfma_i32_16x16x64_i8 v[130:133], v[194:197], v[218:221], v[130:133]
	v_mfma_i32_16x16x64_i8 v[122:125], v[202:205], v[218:221], v[122:125]
	v_mfma_i32_16x16x64_i8 v[114:117], v[194:197], v[226:229], v[114:117]
	v_mfma_i32_16x16x64_i8 v[94:97], v[202:205], v[226:229], v[92:95]
	v_mfma_i32_16x16x64_i8 v[74:77], v[194:197], v[234:237], v[74:77]
	v_mfma_i32_16x16x64_i8 v[66:69], v[202:205], v[234:237], v[66:69]
	s_setprio 0
	s_barrier
	s_add_i32 s8, s72, s57
	v_lshl_add_u64 v[240:241], s[34:35], 0, v[154:155]
	s_mov_b32 m0, s8
	ds_read_b128 v[206:209], v187 offset:16384
	ds_read_b128 v[210:213], v187 offset:17408
	ds_read_b128 v[214:217], v187 offset:18432
	ds_read_b128 v[218:221], v187 offset:19456
	ds_read_b128 v[222:225], v187 offset:20480
	ds_read_b128 v[226:229], v187 offset:21504
	ds_read_b128 v[230:233], v187 offset:22528
	ds_read_b128 v[234:237], v187 offset:23552
	global_load_lds_dwordx4 v[240:241], off
	s_add_i32 m0, s8, 0x2000
	s_add_u32 s8, s34, 0x40000
	v_lshl_add_u64 v[242:243], s[34:35], 0, v[156:157]
	s_addc_u32 s9, s35, 0
	s_add_i32 s54, s73, s57
	global_load_lds_dwordx4 v[242:243], off
	v_lshl_add_u64 v[92:93], s[8:9], 0, v[154:155]
	s_mov_b32 m0, s54
	v_mov_b32_e32 v239, v159
	global_load_lds_dwordx4 v[92:93], off
	v_lshl_add_u64 v[92:93], s[8:9], 0, v[156:157]
	s_add_i32 m0, s54, 0x2000
	v_lshl_add_u64 v[244:245], s[36:37], 0, v[158:159]
	global_load_lds_dwordx4 v[92:93], off
	s_waitcnt vmcnt(6)
	s_waitcnt lgkmcnt(0)
	v_lshl_add_u64 v[238:239], s[36:37], 0, v[238:239]
	s_barrier
; #define PG8_STAGE(bufoff, gbase, voff) do { _Pragma("unroll") for (int _i = 0; _i < 2; ++_i) \
;         __builtin_amdgcn_global_load_lds((const unsigned*)((const char*)(gbase) + (voff)[_i]), (LAS unsigned*)(lds + (bufoff) + ldsw + _i * 8192), 16, 0, 0); } while (0)
; #define PG8_LDA(dst, b, h) do { _Pragma("unroll") for (int m = 0; m < 4; ++m) _Pragma("unroll") for (int k = 0; k < 2; ++k) dst[m][k] = *(const LAS bf16x8*)(lds + PG8_SA(b, h) + aoffL + m * 2048 + k * 1024); } while (0)
; #define PG8_LDB(dst, b, h) do { _Pragma("unroll") for (int n = 0; n < 2; ++n) _Pragma("unroll") for (int k = 0; k < 2; ++k) dst[n][k] = *(const LAS bf16x8*)(lds + PG8_SB(b, h) + boffL + n * 2048 + k * 1024); } while (0)
; #define PG8_WAIT_V(n) asm volatile("s_waitcnt vmcnt(" #n ")" ::: "memory")
; #define PG8_WAIT_L(n) asm volatile("s_waitcnt lgkmcnt(" #n ")" ::: "memory")
; #define PG8_BAR __builtin_amdgcn_s_barrier()
; #define PG8_SCHED __builtin_amdgcn_sched_barrier(0)
;     ...
;             PG8_WAIT_V(8); PG8_WAIT_L(0); PG8_BAR; PG8_MMA(0, 0, At, B0); PG8_MMA(0, 1, At, B1); PG8_BAR; PG8_SCHED;
;             PG8_LDA(At, 0, 1); PG8_STAGE(PG8_SB(0, 0), b2, voffB); PG8_STAGE(PG8_SB(0, 1), b2 + hstep, voffB); PG8_STAGE(PG8_SA(0, 0), a2, x0);
;             PG8_WAIT_V(8); PG8_WAIT_L(0); PG8_BAR; PG8_MMA(1, 0, At, B0); PG8_MMA(1, 1, At, B1); PG8_BAR; PG8_SCHED;
;             PG8_LDB(B0, 1, 0); PG8_LDB(B1, 1, 1); PG8_SCHED; PG8_LDA(At, 1, 0); PG8_STAGE(PG8_SA(0, 1), a2, x1);
;             PG8_WAIT_V(8); PG8_WAIT_L(0); PG8_BAR; PG8_MMA(0, 0, At, B0); PG8_MMA(0, 1, At, B1); PG8_BAR; PG8_SCHED;
	s_setprio 1
	s_waitcnt lgkmcnt(0)
	v_mfma_i32_16x16x64_i8 v[62:65], v[98:101], v[206:209], v[62:65]
	v_mfma_i32_16x16x64_i8 v[54:57], v[106:109], v[206:209], v[54:57]
	v_mfma_i32_16x16x64_i8 v[46:49], v[98:101], v[214:217], v[46:49]
	v_mfma_i32_16x16x64_i8 v[38:41], v[106:109], v[214:217], v[38:41]
	v_mfma_i32_16x16x64_i8 v[22:25], v[98:101], v[222:225], v[22:25]
	v_mfma_i32_16x16x64_i8 v[18:21], v[106:109], v[222:225], v[18:21]
	v_mfma_i32_16x16x64_i8 v[6:9], v[98:101], v[230:233], v[6:9]
	v_mfma_i32_16x16x64_i8 v[2:5], v[106:109], v[230:233], v[2:5]
	v_mfma_i32_16x16x64_i8 v[62:65], v[102:105], v[210:213], v[62:65]
	v_mfma_i32_16x16x64_i8 v[54:57], v[172:175], v[210:213], v[54:57]
	v_mfma_i32_16x16x64_i8 v[46:49], v[102:105], v[218:221], v[46:49]
	v_mfma_i32_16x16x64_i8 v[38:41], v[172:175], v[218:221], v[38:41]
	v_mfma_i32_16x16x64_i8 v[22:25], v[102:105], v[226:229], v[22:25]
	v_mfma_i32_16x16x64_i8 v[18:21], v[172:175], v[226:229], v[18:21]
	v_mfma_i32_16x16x64_i8 v[6:9], v[102:105], v[234:237], v[6:9]
	v_mfma_i32_16x16x64_i8 v[2:5], v[172:175], v[234:237], v[2:5]
	s_setprio 0
	s_setprio 1
	v_mfma_i32_16x16x64_i8 v[58:61], v[176:179], v[206:209], v[58:61]
	v_mfma_i32_16x16x64_i8 v[50:53], v[198:201], v[206:209], v[50:53]
	v_mfma_i32_16x16x64_i8 v[42:45], v[176:179], v[214:217], v[42:45]
	v_mfma_i32_16x16x64_i8 v[30:33], v[198:201], v[214:217], v[30:33]
	v_mfma_i32_16x16x64_i8 v[34:37], v[176:179], v[222:225], v[34:37]
	v_mfma_i32_16x16x64_i8 v[26:29], v[198:201], v[222:225], v[26:29]
	v_mfma_i32_16x16x64_i8 v[14:17], v[176:179], v[230:233], v[14:17]
	v_mfma_i32_16x16x64_i8 v[10:13], v[198:201], v[230:233], v[10:13]
	v_mfma_i32_16x16x64_i8 v[58:61], v[194:197], v[210:213], v[58:61]
	v_mfma_i32_16x16x64_i8 v[50:53], v[202:205], v[210:213], v[50:53]
	v_mfma_i32_16x16x64_i8 v[42:45], v[194:197], v[218:221], v[42:45]
	v_mfma_i32_16x16x64_i8 v[30:33], v[202:205], v[218:221], v[30:33]
	v_mfma_i32_16x16x64_i8 v[34:37], v[194:197], v[226:229], v[34:37]
	v_mfma_i32_16x16x64_i8 v[26:29], v[202:205], v[226:229], v[26:29]
	v_mfma_i32_16x16x64_i8 v[14:17], v[194:197], v[234:237], v[14:17]
	v_mfma_i32_16x16x64_i8 v[10:13], v[202:205], v[234:237], v[10:13]
	s_setprio 0
	s_barrier
	s_add_i32 s8, 0, 0x18000
	v_add_u32_e32 v92, s8, v181
	s_add_i32 s54, 0, 0x1c000
	ds_read_b128 v[98:101], v92
	ds_read_b128 v[102:105], v92 offset:1024
	ds_read_b128 v[106:109], v92 offset:2048
	ds_read_b128 v[172:175], v92 offset:3072
	v_add_u32_e32 v92, s54, v181
	ds_read_b128 v[176:179], v92
	ds_read_b128 v[194:197], v92 offset:1024
	ds_read_b128 v[198:201], v92 offset:2048
	ds_read_b128 v[202:205], v92 offset:3072
	s_mov_b32 m0, s61
	ds_read_b128 v[206:209], v187 offset:32768
	ds_read_b128 v[210:213], v187 offset:33792
	ds_read_b128 v[214:217], v187 offset:34816
	ds_read_b128 v[218:221], v187 offset:35840
	ds_read_b128 v[222:225], v187 offset:36864
	ds_read_b128 v[226:229], v187 offset:37888
	ds_read_b128 v[230:233], v187 offset:38912
	ds_read_b128 v[234:237], v187 offset:39936
	global_load_lds_dwordx4 v158, s[36:37]
	s_mov_b32 m0, s62
	s_nop 0
	global_load_lds_dwordx4 v[238:239], off
	s_mov_b32 m0, s63
	s_nop 0
	global_load_lds_dwordx4 v171, s[36:37]
	s_mov_b32 m0, s64
	s_nop 0
	global_load_lds_dwordx4 v193, s[36:37]
	s_waitcnt vmcnt(8)
	s_waitcnt lgkmcnt(0)
	s_barrier
	s_setprio 1
	s_waitcnt lgkmcnt(0)
	v_mfma_i32_16x16x64_i8 v[150:153], v[98:101], v[206:209], v[150:153]
	v_mfma_i32_16x16x64_i8 v[142:145], v[106:109], v[206:209], v[142:145]
	v_mfma_i32_16x16x64_i8 v[134:137], v[98:101], v[214:217], v[134:137]
	v_mfma_i32_16x16x64_i8 v[126:129], v[106:109], v[214:217], v[126:129]
	v_mfma_i32_16x16x64_i8 v[118:121], v[98:101], v[222:225], v[118:121]
	v_mfma_i32_16x16x64_i8 v[110:113], v[106:109], v[222:225], v[110:113]
	v_mfma_i32_16x16x64_i8 v[88:91], v[98:101], v[230:233], v[88:91]
	v_mfma_i32_16x16x64_i8 v[70:73], v[106:109], v[230:233], v[70:73]
	v_mfma_i32_16x16x64_i8 v[150:153], v[102:105], v[210:213], v[150:153]
	v_mfma_i32_16x16x64_i8 v[142:145], v[172:175], v[210:213], v[142:145]
	v_mfma_i32_16x16x64_i8 v[134:137], v[102:105], v[218:221], v[134:137]
	v_mfma_i32_16x16x64_i8 v[126:129], v[172:175], v[218:221], v[126:129]
	v_mfma_i32_16x16x64_i8 v[118:121], v[102:105], v[226:229], v[118:121]
	v_mfma_i32_16x16x64_i8 v[110:113], v[172:175], v[226:229], v[110:113]
	v_mfma_i32_16x16x64_i8 v[90:93], v[102:105], v[234:237], v[88:91]
	v_mfma_i32_16x16x64_i8 v[70:73], v[172:175], v[234:237], v[70:73]
	s_setprio 0
	s_setprio 1
	v_mfma_i32_16x16x64_i8 v[146:149], v[176:179], v[206:209], v[146:149]
	v_mfma_i32_16x16x64_i8 v[138:141], v[198:201], v[206:209], v[138:141]
	v_mfma_i32_16x16x64_i8 v[130:133], v[176:179], v[214:217], v[130:133]
	v_mfma_i32_16x16x64_i8 v[122:125], v[198:201], v[214:217], v[122:125]
	v_mfma_i32_16x16x64_i8 v[114:117], v[176:179], v[222:225], v[114:117]
	v_mfma_i32_16x16x64_i8 v[94:97], v[198:201], v[222:225], v[94:97]
	v_mfma_i32_16x16x64_i8 v[74:77], v[176:179], v[230:233], v[74:77]
	v_mfma_i32_16x16x64_i8 v[66:69], v[198:201], v[230:233], v[66:69]
	v_mfma_i32_16x16x64_i8 v[146:149], v[194:197], v[210:213], v[146:149]
	v_mfma_i32_16x16x64_i8 v[138:141], v[202:205], v[210:213], v[138:141]
	v_mfma_i32_16x16x64_i8 v[130:133], v[194:197], v[218:221], v[130:133]
	v_mfma_i32_16x16x64_i8 v[122:125], v[202:205], v[218:221], v[122:125]
	v_mfma_i32_16x16x64_i8 v[114:117], v[194:197], v[226:229], v[114:117]
	v_mfma_i32_16x16x64_i8 v[94:97], v[202:205], v[226:229], v[94:97]
	v_mfma_i32_16x16x64_i8 v[74:77], v[194:197], v[234:237], v[74:77]
	v_mfma_i32_16x16x64_i8 v[66:69], v[202:205], v[234:237], v[66:69]
	s_setprio 0
	s_barrier
; #define PG8_STAGE(bufoff, gbase, voff) do { _Pragma("unroll") for (int _i = 0; _i < 2; ++_i) \
;         __builtin_amdgcn_global_load_lds((const unsigned*)((const char*)(gbase) + (voff)[_i]), (LAS unsigned*)(lds + (bufoff) + ldsw + _i * 8192), 16, 0, 0); } while (0)
; #define PG8_LDA(dst, b, h) do { _Pragma("unroll") for (int m = 0; m < 4; ++m) _Pragma("unroll") for (int k = 0; k < 2; ++k) dst[m][k] = *(const LAS bf16x8*)(lds + PG8_SA(b, h) + aoffL + m * 2048 + k * 1024); } while (0)
; #define PG8_WAIT_V(n) asm volatile("s_waitcnt vmcnt(" #n ")" ::: "memory")
; #define PG8_WAIT_L(n) asm volatile("s_waitcnt lgkmcnt(" #n ")" ::: "memory")
; #define PG8_BAR __builtin_amdgcn_s_barrier()
; #define PG8_SCHED __builtin_amdgcn_sched_barrier(0)
;     ...
;             PG8_WAIT_V(8); PG8_WAIT_L(0); PG8_BAR; PG8_MMA(0, 0, At, B0); PG8_MMA(0, 1, At, B1); PG8_BAR; PG8_SCHED;
;             PG8_LDA(At, 1, 1); PG8_STAGE(PG8_SB(1, 0), b3, voffB); PG8_STAGE(PG8_SB(1, 1), b3 + hstep, voffB); PG8_STAGE(PG8_SA(1, 0), a3, x0);
;             PG8_WAIT_V(8); PG8_WAIT_L(0); PG8_BAR; PG8_MMA(1, 0, At, B0); PG8_MMA(1, 1, At, B1); PG8_BAR; PG8_SCHED;
	s_add_i32 s8, s8, s57
	v_lshl_add_u64 v[88:89], v[240:241], 0, s[20:21]
	s_mov_b32 m0, s8
	ds_read_b128 v[206:209], v187 offset:49152
	ds_read_b128 v[210:213], v187 offset:50176
	ds_read_b128 v[214:217], v187 offset:51200
	ds_read_b128 v[218:221], v187 offset:52224
	ds_read_b128 v[222:225], v187 offset:53248
	ds_read_b128 v[226:229], v187 offset:54272
	ds_read_b128 v[230:233], v187 offset:55296
	ds_read_b128 v[234:237], v187 offset:56320
	global_load_lds_dwordx4 v[88:89], off
	s_add_i32 m0, s8, 0x2000
	s_add_u32 s8, s34, 0x40080
	v_lshl_add_u64 v[88:89], v[242:243], 0, s[20:21]
	s_addc_u32 s9, s35, 0
	s_add_i32 s34, s54, s57
	global_load_lds_dwordx4 v[88:89], off
	v_lshl_add_u64 v[88:89], s[8:9], 0, v[154:155]
	s_mov_b32 m0, s34
	s_nop 0
	global_load_lds_dwordx4 v[88:89], off
	v_lshl_add_u64 v[88:89], s[8:9], 0, v[156:157]
	s_add_i32 m0, s34, 0x2000
	s_nop 0
	global_load_lds_dwordx4 v[88:89], off
	v_lshl_add_u64 v[250:251], v[244:245], 0, s[20:21]
	v_lshl_add_u64 v[252:253], v[238:239], 0, s[20:21]
	s_waitcnt vmcnt(6)
	s_waitcnt lgkmcnt(0)
	s_barrier
	s_setprio 1
	s_waitcnt lgkmcnt(0)
	v_mfma_i32_16x16x64_i8 v[62:65], v[98:101], v[206:209], v[62:65]
	v_mfma_i32_16x16x64_i8 v[54:57], v[106:109], v[206:209], v[54:57]
	v_mfma_i32_16x16x64_i8 v[46:49], v[98:101], v[214:217], v[46:49]
	v_mfma_i32_16x16x64_i8 v[38:41], v[106:109], v[214:217], v[38:41]
	v_mfma_i32_16x16x64_i8 v[22:25], v[98:101], v[222:225], v[22:25]
	v_mfma_i32_16x16x64_i8 v[18:21], v[106:109], v[222:225], v[18:21]
	v_mfma_i32_16x16x64_i8 v[6:9], v[98:101], v[230:233], v[6:9]
	v_mfma_i32_16x16x64_i8 v[2:5], v[106:109], v[230:233], v[2:5]
	v_mfma_i32_16x16x64_i8 v[62:65], v[102:105], v[210:213], v[62:65]
	v_mfma_i32_16x16x64_i8 v[54:57], v[172:175], v[210:213], v[54:57]
	v_mfma_i32_16x16x64_i8 v[46:49], v[102:105], v[218:221], v[46:49]
	v_mfma_i32_16x16x64_i8 v[38:41], v[172:175], v[218:221], v[38:41]
	v_mfma_i32_16x16x64_i8 v[22:25], v[102:105], v[226:229], v[22:25]
	v_mfma_i32_16x16x64_i8 v[18:21], v[172:175], v[226:229], v[18:21]
	v_mfma_i32_16x16x64_i8 v[6:9], v[102:105], v[234:237], v[6:9]
	v_mfma_i32_16x16x64_i8 v[2:5], v[172:175], v[234:237], v[2:5]
	s_setprio 0
	s_setprio 1
	v_mfma_i32_16x16x64_i8 v[58:61], v[176:179], v[206:209], v[58:61]
	v_mfma_i32_16x16x64_i8 v[50:53], v[198:201], v[206:209], v[50:53]
	v_mfma_i32_16x16x64_i8 v[42:45], v[176:179], v[214:217], v[42:45]
	v_mfma_i32_16x16x64_i8 v[30:33], v[198:201], v[214:217], v[30:33]
	v_mfma_i32_16x16x64_i8 v[34:37], v[176:179], v[222:225], v[34:37]
	v_mfma_i32_16x16x64_i8 v[26:29], v[198:201], v[222:225], v[26:29]
	v_mfma_i32_16x16x64_i8 v[14:17], v[176:179], v[230:233], v[14:17]
	v_mfma_i32_16x16x64_i8 v[10:13], v[198:201], v[230:233], v[10:13]
	v_mfma_i32_16x16x64_i8 v[58:61], v[194:197], v[210:213], v[58:61]
	v_mfma_i32_16x16x64_i8 v[50:53], v[202:205], v[210:213], v[50:53]
	v_mfma_i32_16x16x64_i8 v[42:45], v[194:197], v[218:221], v[42:45]
	v_mfma_i32_16x16x64_i8 v[30:33], v[202:205], v[218:221], v[30:33]
	v_mfma_i32_16x16x64_i8 v[34:37], v[194:197], v[226:229], v[34:37]
	v_mfma_i32_16x16x64_i8 v[26:29], v[202:205], v[226:229], v[26:29]
	v_mfma_i32_16x16x64_i8 v[14:17], v[194:197], v[234:237], v[14:17]
	v_mfma_i32_16x16x64_i8 v[10:13], v[202:205], v[234:237], v[10:13]
	s_setprio 0
	s_barrier
	s_add_i32 s53, s53, 2
	s_add_u32 s30, s30, 0x100
	s_addc_u32 s31, s31, 0
	s_cmp_gt_u32 s53, 13
	s_cbranch_scc1 .LBB0_2285
